# hot loop tops (four GEMM k-loops, four MoE stream loops) aligned to 64 bytes
# baseline (speedup 1.0000x reference)
; #define PG8_BAR __builtin_amdgcn_s_barrier()
; template <class Epi, class Sched, bool ALIGN_EPI = true, bool SP2 = true>
; __device__ __forceinline__ void gemm_phase(LAS unsigned char* lds, const Dims g, const Sched& S, const Epi& E) {
;     ...
;     for (;;) {
;         const bool has_next = S.next(ui + 1, nxt);
;         const char* nA = has_next ? nxt.A : cA; const char* nB = has_next ? nxt.B : cB;
;         for (int t = 0; t < nt; t += 2) {
;     ...
; #pragma unroll
;         for (int a = 0; a < 2; ++a)
; #pragma unroll
;             for (int b = 0; b < 2; ++b)
; #pragma unroll
;                 for (int m = 0; m < 4; ++m)
; #pragma unroll
;                     for (int n = 0; n < 2; ++n) acc[a][b][m][n] = (f32x4){0.f, 0.f, 0.f, 0.f};
;         cur = nxt; cA = nA; cB = nB; ++ui;
;         if constexpr (ALIGN_EPI) { if (wr == 1) PG8_BAR; }
.LBB0_325:
	s_add_u32 s40, s40, 0x80080
	s_addc_u32 s41, s41, 0
	s_add_u32 s2, s46, 0x100
	v_mov_b32_e32 v2, 0
	s_addc_u32 s3, s47, 0
	s_mov_b32 s31, -2
	v_mov_b32_e32 v3, v2
	v_mov_b32_e32 v4, v2
	v_mov_b32_e32 v5, v2
	v_mov_b32_e32 v6, v2
	v_mov_b32_e32 v7, v2
	v_mov_b32_e32 v8, v2
	v_mov_b32_e32 v9, v2
	v_mov_b32_e32 v10, v2
	v_mov_b32_e32 v11, v2
	v_mov_b32_e32 v12, v2
	v_mov_b32_e32 v13, v2
	v_mov_b32_e32 v18, v2
	v_mov_b32_e32 v19, v2
	v_mov_b32_e32 v20, v2
	v_mov_b32_e32 v21, v2
	v_mov_b32_e32 v26, v2
	v_mov_b32_e32 v27, v2
	v_mov_b32_e32 v28, v2
	v_mov_b32_e32 v29, v2
	v_mov_b32_e32 v34, v2
	v_mov_b32_e32 v35, v2
	v_mov_b32_e32 v36, v2
	v_mov_b32_e32 v37, v2
	v_mov_b32_e32 v42, v2
	v_mov_b32_e32 v43, v2
	v_mov_b32_e32 v44, v2
	v_mov_b32_e32 v45, v2
	v_mov_b32_e32 v50, v2
	v_mov_b32_e32 v51, v2
	v_mov_b32_e32 v52, v2
	v_mov_b32_e32 v53, v2
	v_mov_b32_e32 v14, v2
	v_mov_b32_e32 v15, v2
	v_mov_b32_e32 v16, v2
	v_mov_b32_e32 v17, v2
	v_mov_b32_e32 v22, v2
	v_mov_b32_e32 v23, v2
	v_mov_b32_e32 v24, v2
	v_mov_b32_e32 v25, v2
	v_mov_b32_e32 v30, v2
	v_mov_b32_e32 v31, v2
	v_mov_b32_e32 v32, v2
	v_mov_b32_e32 v33, v2
	v_mov_b32_e32 v38, v2
	v_mov_b32_e32 v39, v2
	v_mov_b32_e32 v40, v2
	v_mov_b32_e32 v41, v2
	v_mov_b32_e32 v46, v2
	v_mov_b32_e32 v47, v2
	v_mov_b32_e32 v48, v2
	v_mov_b32_e32 v49, v2
	v_mov_b32_e32 v54, v2
	v_mov_b32_e32 v55, v2
	v_mov_b32_e32 v56, v2
	v_mov_b32_e32 v57, v2
	v_mov_b32_e32 v58, v2
	v_mov_b32_e32 v59, v2
	v_mov_b32_e32 v60, v2
	v_mov_b32_e32 v61, v2
	v_mov_b32_e32 v62, v2
	v_mov_b32_e32 v63, v2
	v_mov_b32_e32 v64, v2
	v_mov_b32_e32 v65, v2
	v_mov_b32_e32 v66, v2
	v_mov_b32_e32 v67, v2
	v_mov_b32_e32 v68, v2
	v_mov_b32_e32 v69, v2
	v_mov_b32_e32 v70, v2
	v_mov_b32_e32 v71, v2
	v_mov_b32_e32 v72, v2
	v_mov_b32_e32 v73, v2
	v_mov_b32_e32 v74, v2
	v_mov_b32_e32 v75, v2
	v_mov_b32_e32 v76, v2
	v_mov_b32_e32 v77, v2
	v_mov_b32_e32 v82, v2
	v_mov_b32_e32 v83, v2
	v_mov_b32_e32 v84, v2
	v_mov_b32_e32 v85, v2
	v_mov_b32_e32 v92, v2
	v_mov_b32_e32 v93, v2
	v_mov_b32_e32 v94, v2
	v_mov_b32_e32 v95, v2
	v_mov_b32_e32 v100, v2
	v_mov_b32_e32 v101, v2
	v_mov_b32_e32 v102, v2
	v_mov_b32_e32 v103, v2
	v_mov_b32_e32 v108, v2
	v_mov_b32_e32 v109, v2
	v_mov_b32_e32 v110, v2
	v_mov_b32_e32 v111, v2
	v_mov_b32_e32 v120, v2
	v_mov_b32_e32 v121, v2
	v_mov_b32_e32 v122, v2
	v_mov_b32_e32 v123, v2
	v_mov_b32_e32 v78, v2
	v_mov_b32_e32 v79, v2
	v_mov_b32_e32 v80, v2
	v_mov_b32_e32 v81, v2
	v_mov_b32_e32 v86, v2
	v_mov_b32_e32 v87, v2
	v_mov_b32_e32 v88, v2
	v_mov_b32_e32 v89, v2
	v_mov_b32_e32 v96, v2
	v_mov_b32_e32 v97, v2
	v_mov_b32_e32 v98, v2
	v_mov_b32_e32 v99, v2
	v_mov_b32_e32 v104, v2
	v_mov_b32_e32 v105, v2
	v_mov_b32_e32 v106, v2
	v_mov_b32_e32 v107, v2
	v_mov_b32_e32 v112, v2
	v_mov_b32_e32 v113, v2
	v_mov_b32_e32 v114, v2
	v_mov_b32_e32 v115, v2
	v_mov_b32_e32 v116, v2
	v_mov_b32_e32 v117, v2
	v_mov_b32_e32 v118, v2
	v_mov_b32_e32 v119, v2
	v_mov_b32_e32 v124, v2
	v_mov_b32_e32 v125, v2
	v_mov_b32_e32 v126, v2
	v_mov_b32_e32 v127, v2
	v_mov_b32_e32 v128, v2
	v_mov_b32_e32 v129, v2
	v_mov_b32_e32 v130, v2
	v_mov_b32_e32 v131, v2
	.p2alignl 6, 3212836864

; #define PG8_BAR __builtin_amdgcn_s_barrier()
; template <class Epi, class Sched, bool ALIGN_EPI = true, bool SP2 = true>
; __device__ __forceinline__ void gemm_phase(LAS unsigned char* lds, const Dims g, const Sched& S, const Epi& E) {
;     ...
; #pragma unroll
;         for (int a = 0; a < 2; ++a)
; #pragma unroll
;             for (int b = 0; b < 2; ++b)
; #pragma unroll
;                 for (int m = 0; m < 4; ++m)
; #pragma unroll
;                     for (int n = 0; n < 2; ++n) acc[a][b][m][n] = (f32x4){0.f, 0.f, 0.f, 0.f};
;         cur = nxt; cA = nA; cB = nB; ++ui;
;         if constexpr (ALIGN_EPI) { if (wr == 1) PG8_BAR; }
.LBB0_1401:
	s_add_u32 s24, s24, 0x40080
	s_addc_u32 s25, s25, 0
	s_add_u32 s1, s26, 0x100
	v_mov_b32_e32 v2, 0
	s_addc_u32 s2, s27, 0
	s_mov_b32 s3, -2
	v_mov_b32_e32 v3, v2
	v_mov_b32_e32 v4, v2
	v_mov_b32_e32 v5, v2
	v_mov_b32_e32 v6, v2
	v_mov_b32_e32 v7, v2
	v_mov_b32_e32 v8, v2
	v_mov_b32_e32 v9, v2
	v_mov_b32_e32 v18, v2
	v_mov_b32_e32 v19, v2
	v_mov_b32_e32 v20, v2
	v_mov_b32_e32 v21, v2
	v_mov_b32_e32 v22, v2
	v_mov_b32_e32 v23, v2
	v_mov_b32_e32 v24, v2
	v_mov_b32_e32 v25, v2
	v_mov_b32_e32 v34, v2
	v_mov_b32_e32 v35, v2
	v_mov_b32_e32 v36, v2
	v_mov_b32_e32 v37, v2
	v_mov_b32_e32 v38, v2
	v_mov_b32_e32 v39, v2
	v_mov_b32_e32 v40, v2
	v_mov_b32_e32 v41, v2
	v_mov_b32_e32 v50, v2
	v_mov_b32_e32 v51, v2
	v_mov_b32_e32 v52, v2
	v_mov_b32_e32 v53, v2
	v_mov_b32_e32 v54, v2
	v_mov_b32_e32 v55, v2
	v_mov_b32_e32 v56, v2
	v_mov_b32_e32 v57, v2
	v_mov_b32_e32 v10, v2
	v_mov_b32_e32 v11, v2
	v_mov_b32_e32 v12, v2
	v_mov_b32_e32 v13, v2
	v_mov_b32_e32 v14, v2
	v_mov_b32_e32 v15, v2
	v_mov_b32_e32 v16, v2
	v_mov_b32_e32 v17, v2
	v_mov_b32_e32 v26, v2
	v_mov_b32_e32 v27, v2
	v_mov_b32_e32 v28, v2
	v_mov_b32_e32 v29, v2
	v_mov_b32_e32 v30, v2
	v_mov_b32_e32 v31, v2
	v_mov_b32_e32 v32, v2
	v_mov_b32_e32 v33, v2
	v_mov_b32_e32 v42, v2
	v_mov_b32_e32 v43, v2
	v_mov_b32_e32 v44, v2
	v_mov_b32_e32 v45, v2
	v_mov_b32_e32 v46, v2
	v_mov_b32_e32 v47, v2
	v_mov_b32_e32 v48, v2
	v_mov_b32_e32 v49, v2
	v_mov_b32_e32 v58, v2
	v_mov_b32_e32 v59, v2
	v_mov_b32_e32 v60, v2
	v_mov_b32_e32 v61, v2
	v_mov_b32_e32 v62, v2
	v_mov_b32_e32 v63, v2
	v_mov_b32_e32 v64, v2
	v_mov_b32_e32 v65, v2
	v_mov_b32_e32 v66, v2
	v_mov_b32_e32 v67, v2
	v_mov_b32_e32 v68, v2
	v_mov_b32_e32 v69, v2
	v_mov_b32_e32 v70, v2
	v_mov_b32_e32 v71, v2
	v_mov_b32_e32 v72, v2
	v_mov_b32_e32 v73, v2
	v_mov_b32_e32 v82, v2
	v_mov_b32_e32 v83, v2
	v_mov_b32_e32 v84, v2
	v_mov_b32_e32 v85, v2
	v_mov_b32_e32 v86, v2
	v_mov_b32_e32 v87, v2
	v_mov_b32_e32 v88, v2
	v_mov_b32_e32 v89, v2
	v_mov_b32_e32 v100, v2
	v_mov_b32_e32 v101, v2
	v_mov_b32_e32 v102, v2
	v_mov_b32_e32 v103, v2
	v_mov_b32_e32 v104, v2
	v_mov_b32_e32 v105, v2
	v_mov_b32_e32 v106, v2
	v_mov_b32_e32 v107, v2
	v_mov_b32_e32 v116, v2
	v_mov_b32_e32 v117, v2
	v_mov_b32_e32 v118, v2
	v_mov_b32_e32 v119, v2
	v_mov_b32_e32 v120, v2
	v_mov_b32_e32 v121, v2
	v_mov_b32_e32 v122, v2
	v_mov_b32_e32 v123, v2
	v_mov_b32_e32 v74, v2
	v_mov_b32_e32 v75, v2
	v_mov_b32_e32 v76, v2
	v_mov_b32_e32 v77, v2
	v_mov_b32_e32 v78, v2
	v_mov_b32_e32 v79, v2
	v_mov_b32_e32 v80, v2
	v_mov_b32_e32 v81, v2
	v_mov_b32_e32 v92, v2
	v_mov_b32_e32 v93, v2
	v_mov_b32_e32 v94, v2
	v_mov_b32_e32 v95, v2
	v_mov_b32_e32 v96, v2
	v_mov_b32_e32 v97, v2
	v_mov_b32_e32 v98, v2
	v_mov_b32_e32 v99, v2
	v_mov_b32_e32 v108, v2
	v_mov_b32_e32 v109, v2
	v_mov_b32_e32 v110, v2
	v_mov_b32_e32 v111, v2
	v_mov_b32_e32 v112, v2
	v_mov_b32_e32 v113, v2
	v_mov_b32_e32 v114, v2
	v_mov_b32_e32 v115, v2
	v_mov_b32_e32 v124, v2
	v_mov_b32_e32 v125, v2
	v_mov_b32_e32 v126, v2
	v_mov_b32_e32 v127, v2
	v_mov_b32_e32 v132, v2
	v_mov_b32_e32 v133, v2
	v_mov_b32_e32 v134, v2
	v_mov_b32_e32 v135, v2
	.p2alignl 6, 3212836864

; #define PG8_BAR __builtin_amdgcn_s_barrier()
; template <class Epi, class Sched, bool ALIGN_EPI = true, bool SP2 = true>
; __device__ __forceinline__ void gemm_phase(LAS unsigned char* lds, const Dims g, const Sched& S, const Epi& E) {
;     ...
; #pragma unroll
;         for (int a = 0; a < 2; ++a)
; #pragma unroll
;             for (int b = 0; b < 2; ++b)
; #pragma unroll
;                 for (int m = 0; m < 4; ++m)
; #pragma unroll
;                     for (int n = 0; n < 2; ++n) acc[a][b][m][n] = (f32x4){0.f, 0.f, 0.f, 0.f};
;         cur = nxt; cA = nA; cB = nB; ++ui;
;         if constexpr (ALIGN_EPI) { if (wr == 1) PG8_BAR; }
.LBB0_1428:
	s_add_u32 s24, s24, 0x40080
	s_addc_u32 s25, s25, 0
	s_add_u32 s1, s26, 0x100
	v_mov_b32_e32 v2, 0
	s_addc_u32 s2, s27, 0
	s_mov_b32 s3, -2
	v_mov_b32_e32 v3, v2
	v_mov_b32_e32 v4, v2
	v_mov_b32_e32 v5, v2
	v_mov_b32_e32 v6, v2
	v_mov_b32_e32 v7, v2
	v_mov_b32_e32 v8, v2
	v_mov_b32_e32 v9, v2
	v_mov_b32_e32 v18, v2
	v_mov_b32_e32 v19, v2
	v_mov_b32_e32 v20, v2
	v_mov_b32_e32 v21, v2
	v_mov_b32_e32 v22, v2
	v_mov_b32_e32 v23, v2
	v_mov_b32_e32 v24, v2
	v_mov_b32_e32 v25, v2
	v_mov_b32_e32 v34, v2
	v_mov_b32_e32 v35, v2
	v_mov_b32_e32 v36, v2
	v_mov_b32_e32 v37, v2
	v_mov_b32_e32 v38, v2
	v_mov_b32_e32 v39, v2
	v_mov_b32_e32 v40, v2
	v_mov_b32_e32 v41, v2
	v_mov_b32_e32 v50, v2
	v_mov_b32_e32 v51, v2
	v_mov_b32_e32 v52, v2
	v_mov_b32_e32 v53, v2
	v_mov_b32_e32 v54, v2
	v_mov_b32_e32 v55, v2
	v_mov_b32_e32 v56, v2
	v_mov_b32_e32 v57, v2
	v_mov_b32_e32 v10, v2
	v_mov_b32_e32 v11, v2
	v_mov_b32_e32 v12, v2
	v_mov_b32_e32 v13, v2
	v_mov_b32_e32 v14, v2
	v_mov_b32_e32 v15, v2
	v_mov_b32_e32 v16, v2
	v_mov_b32_e32 v17, v2
	v_mov_b32_e32 v26, v2
	v_mov_b32_e32 v27, v2
	v_mov_b32_e32 v28, v2
	v_mov_b32_e32 v29, v2
	v_mov_b32_e32 v30, v2
	v_mov_b32_e32 v31, v2
	v_mov_b32_e32 v32, v2
	v_mov_b32_e32 v33, v2
	v_mov_b32_e32 v42, v2
	v_mov_b32_e32 v43, v2
	v_mov_b32_e32 v44, v2
	v_mov_b32_e32 v45, v2
	v_mov_b32_e32 v46, v2
	v_mov_b32_e32 v47, v2
	v_mov_b32_e32 v48, v2
	v_mov_b32_e32 v49, v2
	v_mov_b32_e32 v58, v2
	v_mov_b32_e32 v59, v2
	v_mov_b32_e32 v60, v2
	v_mov_b32_e32 v61, v2
	v_mov_b32_e32 v62, v2
	v_mov_b32_e32 v63, v2
	v_mov_b32_e32 v64, v2
	v_mov_b32_e32 v65, v2
	v_mov_b32_e32 v66, v2
	v_mov_b32_e32 v67, v2
	v_mov_b32_e32 v68, v2
	v_mov_b32_e32 v69, v2
	v_mov_b32_e32 v70, v2
	v_mov_b32_e32 v71, v2
	v_mov_b32_e32 v72, v2
	v_mov_b32_e32 v73, v2
	v_mov_b32_e32 v82, v2
	v_mov_b32_e32 v83, v2
	v_mov_b32_e32 v84, v2
	v_mov_b32_e32 v85, v2
	v_mov_b32_e32 v86, v2
	v_mov_b32_e32 v87, v2
	v_mov_b32_e32 v88, v2
	v_mov_b32_e32 v89, v2
	v_mov_b32_e32 v100, v2
	v_mov_b32_e32 v101, v2
	v_mov_b32_e32 v102, v2
	v_mov_b32_e32 v103, v2
	v_mov_b32_e32 v104, v2
	v_mov_b32_e32 v105, v2
	v_mov_b32_e32 v106, v2
	v_mov_b32_e32 v107, v2
	v_mov_b32_e32 v116, v2
	v_mov_b32_e32 v117, v2
	v_mov_b32_e32 v118, v2
	v_mov_b32_e32 v119, v2
	v_mov_b32_e32 v120, v2
	v_mov_b32_e32 v121, v2
	v_mov_b32_e32 v122, v2
	v_mov_b32_e32 v123, v2
	v_mov_b32_e32 v74, v2
	v_mov_b32_e32 v75, v2
	v_mov_b32_e32 v76, v2
	v_mov_b32_e32 v77, v2
	v_mov_b32_e32 v78, v2
	v_mov_b32_e32 v79, v2
	v_mov_b32_e32 v80, v2
	v_mov_b32_e32 v81, v2
	v_mov_b32_e32 v92, v2
	v_mov_b32_e32 v93, v2
	v_mov_b32_e32 v94, v2
	v_mov_b32_e32 v95, v2
	v_mov_b32_e32 v96, v2
	v_mov_b32_e32 v97, v2
	v_mov_b32_e32 v98, v2
	v_mov_b32_e32 v99, v2
	v_mov_b32_e32 v108, v2
	v_mov_b32_e32 v109, v2
	v_mov_b32_e32 v110, v2
	v_mov_b32_e32 v111, v2
	v_mov_b32_e32 v112, v2
	v_mov_b32_e32 v113, v2
	v_mov_b32_e32 v114, v2
	v_mov_b32_e32 v115, v2
	v_mov_b32_e32 v124, v2
	v_mov_b32_e32 v125, v2
	v_mov_b32_e32 v126, v2
	v_mov_b32_e32 v127, v2
	v_mov_b32_e32 v136, v2
	v_mov_b32_e32 v137, v2
	v_mov_b32_e32 v138, v2
	v_mov_b32_e32 v139, v2
	.p2alignl 6, 3212836864

; #define PG8_BAR __builtin_amdgcn_s_barrier()
; template <class Epi, class Sched, bool ALIGN_EPI = true, bool SP2 = true>
; __device__ __forceinline__ void gemm_phase(LAS unsigned char* lds, const Dims g, const Sched& S, const Epi& E) {
;     ...
; #pragma unroll
;         for (int a = 0; a < 2; ++a)
; #pragma unroll
;             for (int b = 0; b < 2; ++b)
; #pragma unroll
;                 for (int m = 0; m < 4; ++m)
; #pragma unroll
;                     for (int n = 0; n < 2; ++n) acc[a][b][m][n] = (f32x4){0.f, 0.f, 0.f, 0.f};
;         cur = nxt; cA = nA; cB = nB; ++ui;
;         if constexpr (ALIGN_EPI) { if (wr == 1) PG8_BAR; }
.LBB0_1514:
	s_add_u32 s54, s54, 0x80080
	s_addc_u32 s55, s55, 0
	s_add_u32 s2, s56, 0x100
	v_mov_b32_e32 v2, 0
	s_addc_u32 s3, s57, 0
	s_mov_b32 s35, -2
	v_mov_b32_e32 v3, v2
	v_mov_b32_e32 v4, v2
	v_mov_b32_e32 v5, v2
	v_mov_b32_e32 v6, v2
	v_mov_b32_e32 v7, v2
	v_mov_b32_e32 v8, v2
	v_mov_b32_e32 v9, v2
	v_mov_b32_e32 v18, v2
	v_mov_b32_e32 v19, v2
	v_mov_b32_e32 v20, v2
	v_mov_b32_e32 v21, v2
	v_mov_b32_e32 v22, v2
	v_mov_b32_e32 v23, v2
	v_mov_b32_e32 v24, v2
	v_mov_b32_e32 v25, v2
	v_mov_b32_e32 v34, v2
	v_mov_b32_e32 v35, v2
	v_mov_b32_e32 v36, v2
	v_mov_b32_e32 v37, v2
	v_mov_b32_e32 v38, v2
	v_mov_b32_e32 v39, v2
	v_mov_b32_e32 v40, v2
	v_mov_b32_e32 v41, v2
	v_mov_b32_e32 v50, v2
	v_mov_b32_e32 v51, v2
	v_mov_b32_e32 v52, v2
	v_mov_b32_e32 v53, v2
	v_mov_b32_e32 v54, v2
	v_mov_b32_e32 v55, v2
	v_mov_b32_e32 v56, v2
	v_mov_b32_e32 v57, v2
	v_mov_b32_e32 v10, v2
	v_mov_b32_e32 v11, v2
	v_mov_b32_e32 v12, v2
	v_mov_b32_e32 v13, v2
	v_mov_b32_e32 v14, v2
	v_mov_b32_e32 v15, v2
	v_mov_b32_e32 v16, v2
	v_mov_b32_e32 v17, v2
	v_mov_b32_e32 v26, v2
	v_mov_b32_e32 v27, v2
	v_mov_b32_e32 v28, v2
	v_mov_b32_e32 v29, v2
	v_mov_b32_e32 v30, v2
	v_mov_b32_e32 v31, v2
	v_mov_b32_e32 v32, v2
	v_mov_b32_e32 v33, v2
	v_mov_b32_e32 v42, v2
	v_mov_b32_e32 v43, v2
	v_mov_b32_e32 v44, v2
	v_mov_b32_e32 v45, v2
	v_mov_b32_e32 v46, v2
	v_mov_b32_e32 v47, v2
	v_mov_b32_e32 v48, v2
	v_mov_b32_e32 v49, v2
	v_mov_b32_e32 v58, v2
	v_mov_b32_e32 v59, v2
	v_mov_b32_e32 v60, v2
	v_mov_b32_e32 v61, v2
	v_mov_b32_e32 v62, v2
	v_mov_b32_e32 v63, v2
	v_mov_b32_e32 v64, v2
	v_mov_b32_e32 v65, v2
	v_mov_b32_e32 v66, v2
	v_mov_b32_e32 v67, v2
	v_mov_b32_e32 v68, v2
	v_mov_b32_e32 v69, v2
	v_mov_b32_e32 v70, v2
	v_mov_b32_e32 v71, v2
	v_mov_b32_e32 v72, v2
	v_mov_b32_e32 v73, v2
	v_mov_b32_e32 v82, v2
	v_mov_b32_e32 v83, v2
	v_mov_b32_e32 v84, v2
	v_mov_b32_e32 v85, v2
	v_mov_b32_e32 v86, v2
	v_mov_b32_e32 v87, v2
	v_mov_b32_e32 v88, v2
	v_mov_b32_e32 v89, v2
	v_mov_b32_e32 v100, v2
	v_mov_b32_e32 v101, v2
	v_mov_b32_e32 v102, v2
	v_mov_b32_e32 v103, v2
	v_mov_b32_e32 v104, v2
	v_mov_b32_e32 v105, v2
	v_mov_b32_e32 v106, v2
	v_mov_b32_e32 v107, v2
	v_mov_b32_e32 v116, v2
	v_mov_b32_e32 v117, v2
	v_mov_b32_e32 v118, v2
	v_mov_b32_e32 v119, v2
	v_mov_b32_e32 v120, v2
	v_mov_b32_e32 v121, v2
	v_mov_b32_e32 v122, v2
	v_mov_b32_e32 v123, v2
	v_mov_b32_e32 v74, v2
	v_mov_b32_e32 v75, v2
	v_mov_b32_e32 v76, v2
	v_mov_b32_e32 v77, v2
	v_mov_b32_e32 v78, v2
	v_mov_b32_e32 v79, v2
	v_mov_b32_e32 v80, v2
	v_mov_b32_e32 v81, v2
	v_mov_b32_e32 v92, v2
	v_mov_b32_e32 v93, v2
	v_mov_b32_e32 v94, v2
	v_mov_b32_e32 v95, v2
	v_mov_b32_e32 v96, v2
	v_mov_b32_e32 v97, v2
	v_mov_b32_e32 v98, v2
	v_mov_b32_e32 v99, v2
	v_mov_b32_e32 v108, v2
	v_mov_b32_e32 v109, v2
	v_mov_b32_e32 v110, v2
	v_mov_b32_e32 v111, v2
	v_mov_b32_e32 v112, v2
	v_mov_b32_e32 v113, v2
	v_mov_b32_e32 v114, v2
	v_mov_b32_e32 v115, v2
	v_mov_b32_e32 v124, v2
	v_mov_b32_e32 v125, v2
	v_mov_b32_e32 v126, v2
	v_mov_b32_e32 v127, v2
	v_mov_b32_e32 v128, v2
	v_mov_b32_e32 v129, v2
	v_mov_b32_e32 v130, v2
	v_mov_b32_e32 v131, v2
	.p2alignl 6, 3212836864

; #define LAS __attribute__((address_space(3)))
; #define MS_WLOAD(set, t) do { _Pragma("unroll") for (int r_ = 0; r_ < 4; ++r_) wr[set][r_] = __builtin_bit_cast(f32x4, __builtin_amdgcn_raw_buffer_load_b128(wrs, (int)wvo + r_ * LDW * 4, MS_CL(t) * (64 * LDW * 4), 0)); } while (0)
; #define MS_WCOMMIT(set, bufi) do { LAS unsigned char* wb_ = lds + (bufi) * MS_TILE; _Pragma("unroll") for (int i_ = 0; i_ < 4; ++i_) { \
;             u32x2 p_; p_.x = pk2(wr[set][0][i_], wr[set][1][i_]); p_.y = pk2(wr[set][2][i_], wr[set][3][i_]); \
;             *(LAS u32x2*)(wb_ + ((i_ < 2) ? lw0 : lw1) + i_ * 128) = p_; } } while (0)
; #define MS_XSLOAD(t) do { _Pragma("unroll") for (int i_ = 0; i_ < 6; ++i_) xs[i_] = __builtin_bit_cast(bf16x8, __builtin_amdgcn_raw_buffer_load_b128(xrs, (int)xso[i_], MS_CL(t) * 128, 0)); } while (0)
; #define MS_XSWRITE(bufi) do { _Pragma("unroll") for (int i_ = 0; i_ < 6; ++i_) *(LAS bf16x8*)(xw + (bufi) * MS_XBUF + i_ * 1024 + ((i_ & 1) ? (xwo ^ 64) : xwo)) = xs[i_]; } while (0)
;     ...
;         for (int rp = 0; rp < M; rp += 384) {
;             unsigned xso[6];
; #pragma unroll
;             for (int i = 0; i < 6; ++i) { int tok = rp + wave * 48 + 8 * i + (lane >> 3); tok = min(tok, M - 1); if (VAR == 5) tok &= 15; if (MODE == 0) tok = el[tok]; xso[i] = (unsigned)(tok * LDX * 2 + (lane & 7) * 16); }
;             LAS unsigned char* xw = lds + MS_XOFF + wave * MS_XWAVE; const int xwo = (lane >> 3) * 128 + (((lane & 7) ^ ((lane >> 4) & 3)) << 4);
;             const LAS unsigned char* xr = lds + MS_XOFF + wave * MS_XWAVE + tk * 128 + ((q ^ rd_g) << 4);
;             f32x4 acc[3][8];
; #pragma unroll
;             for (int mt = 0; mt < 3; ++mt)
; #pragma unroll
;                 for (int j = 0; j < 8; ++j) acc[mt][j] = (f32x4){0.f, 0.f, 0.f, 0.f};
;             f32x4 wr[2][4];
;             bf16x8 xs[6];
;     ...
;             const LAS unsigned char* xr1 = lds + MS_XOFF + wave * MS_XWAVE + tk * 128 + (((4 + q) ^ rd_g) << 4);
;             __syncthreads();
;             MS_XSLOAD(0); MS_WLOAD(0, 0); MS_WLOAD(1, 1);
;             MS_WCOMMIT(0, 0); MS_WLOAD(0, 2);
;             MS_XSWRITE(0); MS_XSLOAD(1);
;             __syncthreads();
; #pragma unroll 1
;             for (int t = 0; t < NT; t += 2) { MS_STEP(0, 1, t); MS_STEP(1, 0, t + 1); }
.Lxk_disp:
	s_mov_b32 s67, 0
	s_sub_i32 s81, s28, s31
	s_add_i32 s82, s80, 0x100
	s_cmp_gt_i32 s81, s82
	s_cbranch_scc1 .LBB0_1720
	s_cmp_eq_u32 s84, 0
	s_cbranch_scc1 .Lmoe_k_b
	s_add_i32 s81, s86, 1
	s_sub_i32 s81, s81, s87
	s_cmp_le_i32 s81, s82
	s_cbranch_scc1 .Lmoe_k_b
	.p2alignl 6, 3212836864

; #define LAS __attribute__((address_space(3)))
; #define MS_WLOAD(set, t) do { _Pragma("unroll") for (int r_ = 0; r_ < 4; ++r_) wr[set][r_] = __builtin_bit_cast(f32x4, __builtin_amdgcn_raw_buffer_load_b128(wrs, (int)wvo + r_ * LDW * 4, MS_CL(t) * (64 * LDW * 4), 0)); } while (0)
; #define MS_WCOMMIT(set, bufi) do { LAS unsigned char* wb_ = lds + (bufi) * MS_TILE; _Pragma("unroll") for (int i_ = 0; i_ < 4; ++i_) { \
;             u32x2 p_; p_.x = pk2(wr[set][0][i_], wr[set][1][i_]); p_.y = pk2(wr[set][2][i_], wr[set][3][i_]); \
;             *(LAS u32x2*)(wb_ + ((i_ < 2) ? lw0 : lw1) + i_ * 128) = p_; } } while (0)
; #define MS_XSLOAD(t) do { _Pragma("unroll") for (int i_ = 0; i_ < 6; ++i_) xs[i_] = __builtin_bit_cast(bf16x8, __builtin_amdgcn_raw_buffer_load_b128(xrs, (int)xso[i_], MS_CL(t) * 128, 0)); } while (0)
; #define MS_XSWRITE(bufi) do { _Pragma("unroll") for (int i_ = 0; i_ < 6; ++i_) *(LAS bf16x8*)(xw + (bufi) * MS_XBUF + i_ * 1024 + ((i_ & 1) ? (xwo ^ 64) : xwo)) = xs[i_]; } while (0)
; #define MS_STEP(I, J, t) do { MS_WCOMMIT(J, J); MS_WLOAD(J, (t) + 3); MS_COMPUTE(I); MS_XSWRITE(J); MS_XSLOAD((t) + 2); __syncthreads(); } while (0)
;     ...
;             const LAS unsigned char* xr1 = lds + MS_XOFF + wave * MS_XWAVE + tk * 128 + (((4 + q) ^ rd_g) << 4);
;             __syncthreads();
;             MS_XSLOAD(0); MS_WLOAD(0, 0); MS_WLOAD(1, 1);
;             MS_WCOMMIT(0, 0); MS_WLOAD(0, 2);
;             MS_XSWRITE(0); MS_XSLOAD(1);
;             __syncthreads();
; #pragma unroll 1
;             for (int t = 0; t < NT; t += 2) { MS_STEP(0, 1, t); MS_STEP(1, 0, t + 1); }
.Lxk_nx0:
	s_waitcnt lgkmcnt(9)
	v_mfma_f32_16x16x32_bf16 v[148:151], v[198:201], v[164:167], v[148:151]
	buffer_load_dwordx4 v[124:127], v182, s[4:7], s12 offen
	buffer_load_dwordx4 v[128:131], v183, s[4:7], s12 offen
	buffer_load_dwordx4 v[132:135], v184, s[4:7], s12 offen
	buffer_load_dwordx4 v[136:139], v185, s[4:7], s12 offen
	buffer_load_dwordx4 v[140:143], v186, s[4:7], s12 offen
	buffer_load_dwordx4 v[144:147], v187, s[4:7], s12 offen
	s_min_u32 s12, s0, 27
	s_waitcnt lgkmcnt(0)
	v_mfma_f32_16x16x32_bf16 v[116:119], v[202:205], v[164:167], v[116:119]
	s_barrier
	s_lshl_b32 s12, s12, 17
	v_mfma_f32_16x16x32_bf16 v[92:95], v[206:209], v[164:167], v[92:95]
	s_add_i32 s12, s12, 0x80000
	s_sub_i32 s58, s0, 28
	s_lshl_b32 s58, s58, 17
	s_add_i32 s58, s58, s85
	s_cmp_gt_u32 s0, 27
	s_cselect_b32 s12, s58, s12
	v_mfma_f32_16x16x32_bf16 v[66:69], v[210:213], v[164:167], v[66:69]
	v_cvt_pk_bf16_f32 v164, v96, v100
	v_cvt_pk_bf16_f32 v165, v104, v108
	v_cvt_pk_bf16_f32 v96, v97, v101
	v_cvt_pk_bf16_f32 v97, v105, v109
	ds_write2_b64 v188, v[164:165], v[96:97] offset1:16
	v_cvt_pk_bf16_f32 v96, v98, v102
	v_cvt_pk_bf16_f32 v97, v106, v110
	v_cvt_pk_bf16_f32 v98, v99, v103
	v_cvt_pk_bf16_f32 v99, v107, v111
	ds_write2_b64 v180, v[96:97], v[98:99] offset0:32 offset1:48
	buffer_load_dwordx4 v[96:99], v160, s[8:11], s12 offen nt
	buffer_load_dwordx4 v[100:103], v90, s[8:11], s12 offen nt
	buffer_load_dwordx4 v[104:107], v178, s[8:11], s12 offen nt
	buffer_load_dwordx4 v[108:111], v179, s[8:11], s12 offen nt
	v_mfma_f32_16x16x32_bf16 v[58:61], v[198:201], v[190:193], v[58:61]
	v_mfma_f32_16x16x32_bf16 v[26:29], v[198:201], v[194:197], v[26:29]
	v_mfma_f32_16x16x32_bf16 v[50:53], v[202:205], v[190:193], v[50:53]
	v_mfma_f32_16x16x32_bf16 v[18:21], v[202:205], v[194:197], v[18:21]
	v_mfma_f32_16x16x32_bf16 v[42:45], v[206:209], v[190:193], v[42:45]
	v_mfma_f32_16x16x32_bf16 v[10:13], v[206:209], v[194:197], v[10:13]
	v_mfma_f32_16x16x32_bf16 v[34:37], v[210:213], v[190:193], v[34:37]
	v_mfma_f32_16x16x32_bf16 v[2:5], v[210:213], v[194:197], v[2:5]
	ds_read_b128 v[164:167], v214 offset:38912
	ds_read_b128 v[190:193], v214 offset:40960
	ds_read_b128 v[194:197], v214 offset:43008
	ds_read_b128 v[198:201], v215 offset:16384
	ds_read_b128 v[202:205], v215 offset:18432
	ds_read_b128 v[206:209], v215 offset:20480
	ds_read_b128 v[210:213], v215 offset:22528
	s_waitcnt lgkmcnt(3)
	v_mfma_f32_16x16x32_bf16 v[152:155], v[198:201], v[164:167], v[152:155]
	v_mfma_f32_16x16x32_bf16 v[62:65], v[198:201], v[190:193], v[62:65]
	v_mfma_f32_16x16x32_bf16 v[30:33], v[198:201], v[194:197], v[30:33]
	s_waitcnt lgkmcnt(2)
	v_mfma_f32_16x16x32_bf16 v[120:123], v[202:205], v[164:167], v[120:123]
	v_mfma_f32_16x16x32_bf16 v[54:57], v[202:205], v[190:193], v[54:57]
	v_mfma_f32_16x16x32_bf16 v[22:25], v[202:205], v[194:197], v[22:25]
	s_waitcnt lgkmcnt(1)
	v_mfma_f32_16x16x32_bf16 v[112:115], v[206:209], v[164:167], v[112:115]
	v_mfma_f32_16x16x32_bf16 v[46:49], v[206:209], v[190:193], v[46:49]
	v_mfma_f32_16x16x32_bf16 v[14:17], v[206:209], v[194:197], v[14:17]
	s_waitcnt lgkmcnt(0)
	v_mfma_f32_16x16x32_bf16 v[70:73], v[210:213], v[164:167], v[70:73]
	v_mfma_f32_16x16x32_bf16 v[38:41], v[210:213], v[190:193], v[38:41]
	v_mfma_f32_16x16x32_bf16 v[6:9], v[210:213], v[194:197], v[6:9]
	ds_read_b128 v[198:201], v215 offset:24576
	ds_read_b128 v[202:205], v215 offset:26624
	ds_read_b128 v[206:209], v215 offset:28672
	ds_read_b128 v[210:213], v215 offset:30720
	s_waitcnt lgkmcnt(3)
	v_mfma_f32_16x16x32_bf16 v[148:151], v[198:201], v[164:167], v[148:151]
	v_mfma_f32_16x16x32_bf16 v[58:61], v[198:201], v[190:193], v[58:61]
	v_mfma_f32_16x16x32_bf16 v[26:29], v[198:201], v[194:197], v[26:29]
	s_waitcnt lgkmcnt(2)
	v_mfma_f32_16x16x32_bf16 v[116:119], v[202:205], v[164:167], v[116:119]
	v_mfma_f32_16x16x32_bf16 v[50:53], v[202:205], v[190:193], v[50:53]
	v_mfma_f32_16x16x32_bf16 v[18:21], v[202:205], v[194:197], v[18:21]
	s_waitcnt lgkmcnt(1)
	v_mfma_f32_16x16x32_bf16 v[92:95], v[206:209], v[164:167], v[92:95]
	v_mfma_f32_16x16x32_bf16 v[42:45], v[206:209], v[190:193], v[42:45]
	v_mfma_f32_16x16x32_bf16 v[10:13], v[206:209], v[194:197], v[10:13]
	s_waitcnt lgkmcnt(0)
	v_mfma_f32_16x16x32_bf16 v[66:69], v[210:213], v[164:167], v[66:69]
	v_mfma_f32_16x16x32_bf16 v[34:37], v[210:213], v[190:193], v[34:37]
	v_mfma_f32_16x16x32_bf16 v[2:5], v[210:213], v[194:197], v[2:5]
	ds_read_b128 v[164:167], v216 offset:38912
	ds_read_b128 v[190:193], v216 offset:40960
	ds_read_b128 v[194:197], v216 offset:43008
	ds_read_b128 v[198:201], v217 offset:16384
	ds_read_b128 v[202:205], v217 offset:18432
	ds_read_b128 v[206:209], v217 offset:20480
	ds_read_b128 v[210:213], v217 offset:22528
	s_waitcnt lgkmcnt(3)
	v_mfma_f32_16x16x32_bf16 v[152:155], v[198:201], v[164:167], v[152:155]
	v_mfma_f32_16x16x32_bf16 v[62:65], v[198:201], v[190:193], v[62:65]
	v_mfma_f32_16x16x32_bf16 v[30:33], v[198:201], v[194:197], v[30:33]
	s_waitcnt lgkmcnt(2)
	v_mfma_f32_16x16x32_bf16 v[120:123], v[202:205], v[164:167], v[120:123]
	v_mfma_f32_16x16x32_bf16 v[54:57], v[202:205], v[190:193], v[54:57]
	v_mfma_f32_16x16x32_bf16 v[22:25], v[202:205], v[194:197], v[22:25]
	s_waitcnt lgkmcnt(1)
	v_mfma_f32_16x16x32_bf16 v[112:115], v[206:209], v[164:167], v[112:115]
	v_mfma_f32_16x16x32_bf16 v[46:49], v[206:209], v[190:193], v[46:49]
	v_mfma_f32_16x16x32_bf16 v[14:17], v[206:209], v[194:197], v[14:17]
	s_waitcnt lgkmcnt(0)
	v_mfma_f32_16x16x32_bf16 v[70:73], v[210:213], v[164:167], v[70:73]
	v_mfma_f32_16x16x32_bf16 v[38:41], v[210:213], v[190:193], v[38:41]
	v_mfma_f32_16x16x32_bf16 v[6:9], v[210:213], v[194:197], v[6:9]
	ds_read_b128 v[198:201], v217 offset:24576
	ds_read_b128 v[202:205], v217 offset:26624
	ds_read_b128 v[206:209], v217 offset:28672
	ds_read_b128 v[210:213], v217 offset:30720
	s_lshl_b32 s1, s1, 7
	s_waitcnt vmcnt(9)
	ds_write_b128 v189, v[124:127] offset:32768
	s_waitcnt vmcnt(8)
	ds_write_b128 v181, v[128:131] offset:33792
	s_waitcnt vmcnt(7)
	ds_write_b128 v189, v[132:135] offset:34816
	s_waitcnt vmcnt(6)
	ds_write_b128 v181, v[136:139] offset:35840
	s_waitcnt vmcnt(5)
	ds_write_b128 v189, v[140:143] offset:36864
	s_waitcnt vmcnt(4)
	ds_write_b128 v181, v[144:147] offset:37888
	s_addk_i32 s1, 0x180
	s_cmp_eq_u32 s0, 30
	s_cselect_b32 s58, s84, 0
	s_cmp_lg_u32 s58, 0
	s_cselect_b32 s1, 0x80, s1
	buffer_load_dwordx4 v[132:135], v182, s[4:7], s1 offen
	buffer_load_dwordx4 v[124:127], v183, s[4:7], s1 offen
	buffer_load_dwordx4 v[140:143], v184, s[4:7], s1 offen
	buffer_load_dwordx4 v[144:147], v185, s[4:7], s1 offen
	buffer_load_dwordx4 v[128:131], v186, s[4:7], s1 offen
	buffer_load_dwordx4 v[136:139], v187, s[4:7], s1 offen
	s_waitcnt lgkmcnt(9)
	v_mfma_f32_16x16x32_bf16 v[148:151], v[198:201], v[164:167], v[148:151]
	s_cmp_gt_u32 s0, 29
	s_waitcnt lgkmcnt(0)
	s_barrier
; #define LAS __attribute__((address_space(3)))
; #define MS_WLOAD(set, t) do { _Pragma("unroll") for (int r_ = 0; r_ < 4; ++r_) wr[set][r_] = __builtin_bit_cast(f32x4, __builtin_amdgcn_raw_buffer_load_b128(wrs, (int)wvo + r_ * LDW * 4, MS_CL(t) * (64 * LDW * 4), 0)); } while (0)
; #define MS_WCOMMIT(set, bufi) do { LAS unsigned char* wb_ = lds + (bufi) * MS_TILE; _Pragma("unroll") for (int i_ = 0; i_ < 4; ++i_) { \
;             u32x2 p_; p_.x = pk2(wr[set][0][i_], wr[set][1][i_]); p_.y = pk2(wr[set][2][i_], wr[set][3][i_]); \
;             *(LAS u32x2*)(wb_ + ((i_ < 2) ? lw0 : lw1) + i_ * 128) = p_; } } while (0)
; #define MS_XSLOAD(t) do { _Pragma("unroll") for (int i_ = 0; i_ < 6; ++i_) xs[i_] = __builtin_bit_cast(bf16x8, __builtin_amdgcn_raw_buffer_load_b128(xrs, (int)xso[i_], MS_CL(t) * 128, 0)); } while (0)
; #define MS_XSWRITE(bufi) do { _Pragma("unroll") for (int i_ = 0; i_ < 6; ++i_) *(LAS bf16x8*)(xw + (bufi) * MS_XBUF + i_ * 1024 + ((i_ & 1) ? (xwo ^ 64) : xwo)) = xs[i_]; } while (0)
; #define MS_STEP(I, J, t) do { MS_WCOMMIT(J, J); MS_WLOAD(J, (t) + 3); MS_COMPUTE(I); MS_XSWRITE(J); MS_XSLOAD((t) + 2); __syncthreads(); } while (0)
;     ...
;             const LAS unsigned char* xr1 = lds + MS_XOFF + wave * MS_XWAVE + tk * 128 + (((4 + q) ^ rd_g) << 4);
;             __syncthreads();
;             MS_XSLOAD(0); MS_WLOAD(0, 0); MS_WLOAD(1, 1);
;             MS_WCOMMIT(0, 0); MS_WLOAD(0, 2);
;             MS_XSWRITE(0); MS_XSLOAD(1);
;             __syncthreads();
; #pragma unroll 1
;             for (int t = 0; t < NT; t += 2) { MS_STEP(0, 1, t); MS_STEP(1, 0, t + 1); }
	v_mfma_f32_16x16x32_bf16 v[58:61], v[198:201], v[190:193], v[58:61]
	v_mfma_f32_16x16x32_bf16 v[26:29], v[198:201], v[194:197], v[26:29]
	v_mfma_f32_16x16x32_bf16 v[116:119], v[202:205], v[164:167], v[116:119]
	v_mfma_f32_16x16x32_bf16 v[50:53], v[202:205], v[190:193], v[50:53]
	v_mfma_f32_16x16x32_bf16 v[18:21], v[202:205], v[194:197], v[18:21]
	v_mfma_f32_16x16x32_bf16 v[92:95], v[206:209], v[164:167], v[92:95]
	v_mfma_f32_16x16x32_bf16 v[42:45], v[206:209], v[190:193], v[42:45]
	v_mfma_f32_16x16x32_bf16 v[10:13], v[206:209], v[194:197], v[10:13]
	v_mfma_f32_16x16x32_bf16 v[66:69], v[210:213], v[164:167], v[66:69]
	v_mfma_f32_16x16x32_bf16 v[34:37], v[210:213], v[190:193], v[34:37]
	v_mfma_f32_16x16x32_bf16 v[2:5], v[210:213], v[194:197], v[2:5]
	s_cbranch_scc0 .LBB0_1720
	s_branch .Lmoe_k_done
	.p2alignl 6, 3212836864

; #define LAS __attribute__((address_space(3)))
; #define MS_WLOAD(set, t) do { _Pragma("unroll") for (int r_ = 0; r_ < 4; ++r_) wr[set][r_] = __builtin_bit_cast(f32x4, __builtin_amdgcn_raw_buffer_load_b128(wrs, (int)wvo + r_ * LDW * 4, MS_CL(t) * (64 * LDW * 4), 0)); } while (0)
; #define MS_WCOMMIT(set, bufi) do { LAS unsigned char* wb_ = lds + (bufi) * MS_TILE; _Pragma("unroll") for (int i_ = 0; i_ < 4; ++i_) { \
;             u32x2 p_; p_.x = pk2(wr[set][0][i_], wr[set][1][i_]); p_.y = pk2(wr[set][2][i_], wr[set][3][i_]); \
;             *(LAS u32x2*)(wb_ + ((i_ < 2) ? lw0 : lw1) + i_ * 128) = p_; } } while (0)
; #define MS_XSLOAD(t) do { _Pragma("unroll") for (int i_ = 0; i_ < 6; ++i_) xs[i_] = __builtin_bit_cast(bf16x8, __builtin_amdgcn_raw_buffer_load_b128(xrs, (int)xso[i_], MS_CL(t) * 128, 0)); } while (0)
; #define MS_XSWRITE(bufi) do { _Pragma("unroll") for (int i_ = 0; i_ < 6; ++i_) *(LAS bf16x8*)(xw + (bufi) * MS_XBUF + i_ * 1024 + ((i_ & 1) ? (xwo ^ 64) : xwo)) = xs[i_]; } while (0)
;     ...
;         for (int rp = 0; rp < M; rp += 384) {
;             unsigned xso[6];
; #pragma unroll
;             for (int i = 0; i < 6; ++i) { int tok = rp + wave * 48 + 8 * i + (lane >> 3); tok = min(tok, M - 1); if (VAR == 5) tok &= 15; if (MODE == 0) tok = el[tok]; xso[i] = (unsigned)(tok * LDX * 2 + (lane & 7) * 16); }
;             LAS unsigned char* xw = lds + MS_XOFF + wave * MS_XWAVE; const int xwo = (lane >> 3) * 128 + (((lane & 7) ^ ((lane >> 4) & 3)) << 4);
;             const LAS unsigned char* xr = lds + MS_XOFF + wave * MS_XWAVE + tk * 128 + ((q ^ rd_g) << 4);
;             f32x4 acc[3][8];
; #pragma unroll
;             for (int mt = 0; mt < 3; ++mt)
; #pragma unroll
;                 for (int j = 0; j < 8; ++j) acc[mt][j] = (f32x4){0.f, 0.f, 0.f, 0.f};
;             f32x4 wr[2][4];
;             bf16x8 xs[6];
;     ...
;             const LAS unsigned char* xr1 = lds + MS_XOFF + wave * MS_XWAVE + tk * 128 + (((4 + q) ^ rd_g) << 4);
;             __syncthreads();
;             MS_XSLOAD(0); MS_WLOAD(0, 0); MS_WLOAD(1, 1);
;             MS_WCOMMIT(0, 0); MS_WLOAD(0, 2);
;             MS_XSWRITE(0); MS_XSLOAD(1);
;             __syncthreads();
; #pragma unroll 1
;             for (int t = 0; t < NT; t += 2) { MS_STEP(0, 1, t); MS_STEP(1, 0, t + 1); }
.Lxl_disp:
	s_mov_b32 s67, 0
	s_sub_i32 s81, s30, s31
	s_add_i32 s82, s80, 0x100
	s_cmp_gt_i32 s81, s82
	s_cbranch_scc1 .LBB0_1785
	s_cmp_eq_u32 s84, 0
	s_cbranch_scc1 .Lmoe_l_b
	s_add_i32 s81, s86, 1
	s_sub_i32 s81, s81, s87
	s_cmp_le_i32 s81, s82
	s_cbranch_scc1 .Lmoe_l_b
	.p2alignl 6, 3212836864

; #define LAS __attribute__((address_space(3)))
; #define MS_WLOAD(set, t) do { _Pragma("unroll") for (int r_ = 0; r_ < 4; ++r_) wr[set][r_] = __builtin_bit_cast(f32x4, __builtin_amdgcn_raw_buffer_load_b128(wrs, (int)wvo + r_ * LDW * 4, MS_CL(t) * (64 * LDW * 4), 0)); } while (0)
; #define MS_WCOMMIT(set, bufi) do { LAS unsigned char* wb_ = lds + (bufi) * MS_TILE; _Pragma("unroll") for (int i_ = 0; i_ < 4; ++i_) { \
;             u32x2 p_; p_.x = pk2(wr[set][0][i_], wr[set][1][i_]); p_.y = pk2(wr[set][2][i_], wr[set][3][i_]); \
;             *(LAS u32x2*)(wb_ + ((i_ < 2) ? lw0 : lw1) + i_ * 128) = p_; } } while (0)
; #define MS_XSLOAD(t) do { _Pragma("unroll") for (int i_ = 0; i_ < 6; ++i_) xs[i_] = __builtin_bit_cast(bf16x8, __builtin_amdgcn_raw_buffer_load_b128(xrs, (int)xso[i_], MS_CL(t) * 128, 0)); } while (0)
; #define MS_XSWRITE(bufi) do { _Pragma("unroll") for (int i_ = 0; i_ < 6; ++i_) *(LAS bf16x8*)(xw + (bufi) * MS_XBUF + i_ * 1024 + ((i_ & 1) ? (xwo ^ 64) : xwo)) = xs[i_]; } while (0)
; #define MS_STEP(I, J, t) do { MS_WCOMMIT(J, J); MS_WLOAD(J, (t) + 3); MS_COMPUTE(I); MS_XSWRITE(J); MS_XSLOAD((t) + 2); __syncthreads(); } while (0)
;     ...
;             const LAS unsigned char* xr1 = lds + MS_XOFF + wave * MS_XWAVE + tk * 128 + (((4 + q) ^ rd_g) << 4);
;             __syncthreads();
;             MS_XSLOAD(0); MS_WLOAD(0, 0); MS_WLOAD(1, 1);
;             MS_WCOMMIT(0, 0); MS_WLOAD(0, 2);
;             MS_XSWRITE(0); MS_XSLOAD(1);
;             __syncthreads();
; #pragma unroll 1
;             for (int t = 0; t < NT; t += 2) { MS_STEP(0, 1, t); MS_STEP(1, 0, t + 1); }
.Lxl_nx0:
	s_waitcnt lgkmcnt(9)
	v_mfma_f32_16x16x32_bf16 v[136:139], v[198:201], v[164:167], v[136:139]
	buffer_load_dwordx4 v[92:95], v182, s[4:7], s33 offen
	buffer_load_dwordx4 v[100:103], v183, s[4:7], s33 offen
	buffer_load_dwordx4 v[104:107], v184, s[4:7], s33 offen
	buffer_load_dwordx4 v[108:111], v185, s[4:7], s33 offen
	buffer_load_dwordx4 v[112:115], v186, s[4:7], s33 offen
	buffer_load_dwordx4 v[116:119], v187, s[4:7], s33 offen
	s_min_u32 s33, s2, 3
	s_waitcnt lgkmcnt(0)
	v_mfma_f32_16x16x32_bf16 v[132:135], v[202:205], v[164:167], v[132:135]
	s_barrier
	s_lshl_b32 s33, s33, 19
	v_mfma_f32_16x16x32_bf16 v[128:131], v[206:209], v[164:167], v[128:131]
	s_bitset1_b32 s33, 21
	s_sub_i32 s40, s2, 4
	s_lshl_b32 s40, s40, 19
	s_add_i32 s40, s40, s85
	s_cmp_gt_u32 s2, 3
	s_cselect_b32 s33, s40, s33
	v_mfma_f32_16x16x32_bf16 v[124:127], v[210:213], v[164:167], v[124:127]
	v_cvt_pk_bf16_f32 v164, v18, v22
	v_cvt_pk_bf16_f32 v165, v26, v30
	v_cvt_pk_bf16_f32 v18, v19, v23
	v_cvt_pk_bf16_f32 v19, v27, v31
	ds_write2_b64 v188, v[164:165], v[18:19] offset1:16
	v_cvt_pk_bf16_f32 v18, v20, v24
	v_cvt_pk_bf16_f32 v19, v28, v32
	v_cvt_pk_bf16_f32 v20, v21, v25
	v_cvt_pk_bf16_f32 v21, v29, v33
	ds_write2_b64 v180, v[18:19], v[20:21] offset0:32 offset1:48
	buffer_load_dwordx4 v[18:21], v160, s[8:11], s33 offen nt
	buffer_load_dwordx4 v[22:25], v90, s[8:11], s33 offen nt
	buffer_load_dwordx4 v[26:29], v178, s[8:11], s33 offen nt
	buffer_load_dwordx4 v[30:33], v179, s[8:11], s33 offen nt
	v_mfma_f32_16x16x32_bf16 v[78:81], v[198:201], v[190:193], v[78:81]
	v_mfma_f32_16x16x32_bf16 v[46:49], v[198:201], v[194:197], v[46:49]
	v_mfma_f32_16x16x32_bf16 v[74:77], v[202:205], v[190:193], v[74:77]
	v_mfma_f32_16x16x32_bf16 v[42:45], v[202:205], v[194:197], v[42:45]
	v_mfma_f32_16x16x32_bf16 v[70:73], v[206:209], v[190:193], v[70:73]
	v_mfma_f32_16x16x32_bf16 v[38:41], v[206:209], v[194:197], v[38:41]
	v_mfma_f32_16x16x32_bf16 v[66:69], v[210:213], v[190:193], v[66:69]
	v_mfma_f32_16x16x32_bf16 v[34:37], v[210:213], v[194:197], v[34:37]
	ds_read_b128 v[164:167], v214 offset:38912
	ds_read_b128 v[190:193], v214 offset:40960
	ds_read_b128 v[194:197], v214 offset:43008
	ds_read_b128 v[198:201], v215 offset:16384
	ds_read_b128 v[202:205], v215 offset:18432
	ds_read_b128 v[206:209], v215 offset:20480
	ds_read_b128 v[210:213], v215 offset:22528
	s_waitcnt lgkmcnt(3)
	v_mfma_f32_16x16x32_bf16 v[152:155], v[198:201], v[164:167], v[152:155]
	v_mfma_f32_16x16x32_bf16 v[120:123], v[198:201], v[190:193], v[120:123]
	v_mfma_f32_16x16x32_bf16 v[62:65], v[198:201], v[194:197], v[62:65]
	s_waitcnt lgkmcnt(2)
	v_mfma_f32_16x16x32_bf16 v[148:151], v[202:205], v[164:167], v[148:151]
	v_mfma_f32_16x16x32_bf16 v[96:99], v[202:205], v[190:193], v[96:99]
	v_mfma_f32_16x16x32_bf16 v[58:61], v[202:205], v[194:197], v[58:61]
	s_waitcnt lgkmcnt(1)
	v_mfma_f32_16x16x32_bf16 v[144:147], v[206:209], v[164:167], v[144:147]
	v_mfma_f32_16x16x32_bf16 v[86:89], v[206:209], v[190:193], v[86:89]
	v_mfma_f32_16x16x32_bf16 v[54:57], v[206:209], v[194:197], v[54:57]
	s_waitcnt lgkmcnt(0)
	v_mfma_f32_16x16x32_bf16 v[140:143], v[210:213], v[164:167], v[140:143]
	v_mfma_f32_16x16x32_bf16 v[82:85], v[210:213], v[190:193], v[82:85]
	v_mfma_f32_16x16x32_bf16 v[50:53], v[210:213], v[194:197], v[50:53]
	ds_read_b128 v[198:201], v215 offset:24576
	ds_read_b128 v[202:205], v215 offset:26624
	ds_read_b128 v[206:209], v215 offset:28672
	ds_read_b128 v[210:213], v215 offset:30720
	s_waitcnt lgkmcnt(3)
	v_mfma_f32_16x16x32_bf16 v[136:139], v[198:201], v[164:167], v[136:139]
	v_mfma_f32_16x16x32_bf16 v[78:81], v[198:201], v[190:193], v[78:81]
	v_mfma_f32_16x16x32_bf16 v[46:49], v[198:201], v[194:197], v[46:49]
	s_waitcnt lgkmcnt(2)
	v_mfma_f32_16x16x32_bf16 v[132:135], v[202:205], v[164:167], v[132:135]
	v_mfma_f32_16x16x32_bf16 v[74:77], v[202:205], v[190:193], v[74:77]
	v_mfma_f32_16x16x32_bf16 v[42:45], v[202:205], v[194:197], v[42:45]
	s_waitcnt lgkmcnt(1)
	v_mfma_f32_16x16x32_bf16 v[128:131], v[206:209], v[164:167], v[128:131]
	v_mfma_f32_16x16x32_bf16 v[70:73], v[206:209], v[190:193], v[70:73]
	v_mfma_f32_16x16x32_bf16 v[38:41], v[206:209], v[194:197], v[38:41]
	s_waitcnt lgkmcnt(0)
	v_mfma_f32_16x16x32_bf16 v[124:127], v[210:213], v[164:167], v[124:127]
	v_mfma_f32_16x16x32_bf16 v[66:69], v[210:213], v[190:193], v[66:69]
	v_mfma_f32_16x16x32_bf16 v[34:37], v[210:213], v[194:197], v[34:37]
	ds_read_b128 v[164:167], v216 offset:38912
	ds_read_b128 v[190:193], v216 offset:40960
	ds_read_b128 v[194:197], v216 offset:43008
	ds_read_b128 v[198:201], v217 offset:16384
	ds_read_b128 v[202:205], v217 offset:18432
	ds_read_b128 v[206:209], v217 offset:20480
	ds_read_b128 v[210:213], v217 offset:22528
	s_waitcnt lgkmcnt(3)
	v_mfma_f32_16x16x32_bf16 v[152:155], v[198:201], v[164:167], v[152:155]
	v_mfma_f32_16x16x32_bf16 v[120:123], v[198:201], v[190:193], v[120:123]
	v_mfma_f32_16x16x32_bf16 v[62:65], v[198:201], v[194:197], v[62:65]
	s_waitcnt lgkmcnt(2)
	v_mfma_f32_16x16x32_bf16 v[148:151], v[202:205], v[164:167], v[148:151]
	v_mfma_f32_16x16x32_bf16 v[96:99], v[202:205], v[190:193], v[96:99]
	v_mfma_f32_16x16x32_bf16 v[58:61], v[202:205], v[194:197], v[58:61]
	s_waitcnt lgkmcnt(1)
	v_mfma_f32_16x16x32_bf16 v[144:147], v[206:209], v[164:167], v[144:147]
	v_mfma_f32_16x16x32_bf16 v[86:89], v[206:209], v[190:193], v[86:89]
	v_mfma_f32_16x16x32_bf16 v[54:57], v[206:209], v[194:197], v[54:57]
	s_waitcnt lgkmcnt(0)
	v_mfma_f32_16x16x32_bf16 v[140:143], v[210:213], v[164:167], v[140:143]
	v_mfma_f32_16x16x32_bf16 v[82:85], v[210:213], v[190:193], v[82:85]
	v_mfma_f32_16x16x32_bf16 v[50:53], v[210:213], v[194:197], v[50:53]
	ds_read_b128 v[198:201], v217 offset:24576
	ds_read_b128 v[202:205], v217 offset:26624
	ds_read_b128 v[206:209], v217 offset:28672
	ds_read_b128 v[210:213], v217 offset:30720
	s_lshl_b32 s3, s3, 7
	s_waitcnt vmcnt(9)
	ds_write_b128 v189, v[92:95] offset:32768
	s_waitcnt vmcnt(8)
	ds_write_b128 v181, v[100:103] offset:33792
	s_waitcnt vmcnt(7)
	ds_write_b128 v189, v[104:107] offset:34816
	s_waitcnt vmcnt(6)
	ds_write_b128 v181, v[108:111] offset:35840
	s_waitcnt vmcnt(5)
	ds_write_b128 v189, v[112:115] offset:36864
	s_waitcnt vmcnt(4)
	ds_write_b128 v181, v[116:119] offset:37888
	s_addk_i32 s3, 0x180
	s_cmp_eq_u32 s2, 6
	s_cselect_b32 s40, s84, 0
	s_cmp_lg_u32 s40, 0
	s_cselect_b32 s3, 0x80, s3
	buffer_load_dwordx4 v[104:107], v182, s[4:7], s3 offen
	buffer_load_dwordx4 v[92:95], v183, s[4:7], s3 offen
	buffer_load_dwordx4 v[112:115], v184, s[4:7], s3 offen
	buffer_load_dwordx4 v[116:119], v185, s[4:7], s3 offen
	buffer_load_dwordx4 v[100:103], v186, s[4:7], s3 offen
	buffer_load_dwordx4 v[108:111], v187, s[4:7], s3 offen
	s_waitcnt lgkmcnt(9)
	v_mfma_f32_16x16x32_bf16 v[136:139], v[198:201], v[164:167], v[136:139]
	s_cmp_gt_u32 s2, 5
	s_waitcnt lgkmcnt(0)
	s_barrier
; #define LAS __attribute__((address_space(3)))
; #define MS_WLOAD(set, t) do { _Pragma("unroll") for (int r_ = 0; r_ < 4; ++r_) wr[set][r_] = __builtin_bit_cast(f32x4, __builtin_amdgcn_raw_buffer_load_b128(wrs, (int)wvo + r_ * LDW * 4, MS_CL(t) * (64 * LDW * 4), 0)); } while (0)
; #define MS_WCOMMIT(set, bufi) do { LAS unsigned char* wb_ = lds + (bufi) * MS_TILE; _Pragma("unroll") for (int i_ = 0; i_ < 4; ++i_) { \
;             u32x2 p_; p_.x = pk2(wr[set][0][i_], wr[set][1][i_]); p_.y = pk2(wr[set][2][i_], wr[set][3][i_]); \
;             *(LAS u32x2*)(wb_ + ((i_ < 2) ? lw0 : lw1) + i_ * 128) = p_; } } while (0)
; #define MS_XSLOAD(t) do { _Pragma("unroll") for (int i_ = 0; i_ < 6; ++i_) xs[i_] = __builtin_bit_cast(bf16x8, __builtin_amdgcn_raw_buffer_load_b128(xrs, (int)xso[i_], MS_CL(t) * 128, 0)); } while (0)
; #define MS_XSWRITE(bufi) do { _Pragma("unroll") for (int i_ = 0; i_ < 6; ++i_) *(LAS bf16x8*)(xw + (bufi) * MS_XBUF + i_ * 1024 + ((i_ & 1) ? (xwo ^ 64) : xwo)) = xs[i_]; } while (0)
; #define MS_STEP(I, J, t) do { MS_WCOMMIT(J, J); MS_WLOAD(J, (t) + 3); MS_COMPUTE(I); MS_XSWRITE(J); MS_XSLOAD((t) + 2); __syncthreads(); } while (0)
;     ...
;             const LAS unsigned char* xr1 = lds + MS_XOFF + wave * MS_XWAVE + tk * 128 + (((4 + q) ^ rd_g) << 4);
;             __syncthreads();
;             MS_XSLOAD(0); MS_WLOAD(0, 0); MS_WLOAD(1, 1);
;             MS_WCOMMIT(0, 0); MS_WLOAD(0, 2);
;             MS_XSWRITE(0); MS_XSLOAD(1);
;             __syncthreads();
; #pragma unroll 1
;             for (int t = 0; t < NT; t += 2) { MS_STEP(0, 1, t); MS_STEP(1, 0, t + 1); }
	v_mfma_f32_16x16x32_bf16 v[78:81], v[198:201], v[190:193], v[78:81]
	v_mfma_f32_16x16x32_bf16 v[46:49], v[198:201], v[194:197], v[46:49]
	v_mfma_f32_16x16x32_bf16 v[132:135], v[202:205], v[164:167], v[132:135]
	v_mfma_f32_16x16x32_bf16 v[74:77], v[202:205], v[190:193], v[74:77]
	v_mfma_f32_16x16x32_bf16 v[42:45], v[202:205], v[194:197], v[42:45]
	v_mfma_f32_16x16x32_bf16 v[128:131], v[206:209], v[164:167], v[128:131]
	v_mfma_f32_16x16x32_bf16 v[70:73], v[206:209], v[190:193], v[70:73]
	v_mfma_f32_16x16x32_bf16 v[38:41], v[206:209], v[194:197], v[38:41]
	v_mfma_f32_16x16x32_bf16 v[124:127], v[210:213], v[164:167], v[124:127]
	v_mfma_f32_16x16x32_bf16 v[66:69], v[210:213], v[190:193], v[66:69]
	v_mfma_f32_16x16x32_bf16 v[34:37], v[210:213], v[194:197], v[34:37]
	s_cbranch_scc0 .LBB0_1785
	s_branch .Lmoe_l_done
	.p2alignl 6, 3212836864
